# speedup vs baseline: 1.0119x; 1.0085x over previous
_Z8dog_mainPKfS0_S0_S0_S0_S0_S0_Pf:
	s_load_dwordx8 s[12:19], s[0:1], 0x0
	s_load_dwordx8 s[20:27], s[0:1], 0x20
	s_and_b32 s3, s2, 7
	s_lshl_b32 s3, s3, 5
	s_lshr_b32 s4, s2, 3
	s_add_i32 s4, s3, s4
	s_and_b32 s6, s4, 3
	s_lshr_b32 s7, s4, 2
	s_mov_b32 s5, 0
	s_lshl_b64 s[8:9], s[4:5], 18
	v_and_b32_e32 v1, 63, v0
	v_lshrrev_b32_e32 v2, 6, v0
	v_and_b32_e32 v3, 15, v0
	v_and_b32_e32 v7, 31, v0
	v_lshl_or_b32 v5, v2, 5, v7
	v_lshlrev_b32_e32 v5, 2, v5
	v_mov_b32_e32 v4, v5
	v_lshlrev_b32_e32 v6, 4, v1
	v_lshl_or_b32 v6, v2, 12, v6
	v_bfe_u32 v7, v0, 4, 2
	s_waitcnt lgkmcnt(0)
	global_load_dword v32, v4, s[18:19]
	global_load_dword v33, v4, s[20:21]
	global_load_dword v34, v4, s[22:23]
	global_load_dword v35, v4, s[24:25]
	global_load_dword v36, v4, s[14:15]
	global_load_dword v37, v4, s[16:17]
	s_add_u32 s12, s12, s8
	s_addc_u32 s13, s13, s9
	global_load_dwordx4 v[128:131], v6, s[12:13] offset:0 nt
	global_load_dwordx4 v[132:135], v6, s[12:13] offset:1024 nt
	global_load_dwordx4 v[136:139], v6, s[12:13] offset:2048 nt
	global_load_dwordx4 v[140:143], v6, s[12:13] offset:3072 nt
	v_and_b32_e32 v16, 1, v0
	v_cmp_eq_u32_e64 s[30:31], 0, v16
	v_and_b32_e32 v17, 2, v0
	v_cmp_eq_u32_e64 s[32:33], 0, v17
	v_and_b32_e32 v16, 3, v0
	v_lshrrev_b32_e32 v17, 2, v1
	v_lshlrev_b32_e32 v16, 5, v16
	v_lshl_add_u32 v16, v17, 1, v16
	v_lshrrev_b32_e32 v17, 1, v2
	s_movk_i32 s10, 0x110
	v_mad_u32_u24 v16, v17, s10, v16
	v_and_b32_e32 v17, 1, v2
	v_lshl_add_u32 v14, v17, 7, v16
	v_lshlrev_b32_e32 v17, 4, v7
	v_mad_u32_u24 v15, v3, s10, v17
	s_lshl_b32 s11, s6, 5
	v_lshl_add_u32 v18, v7, 2, s11
	v_cvt_f32_u32_e32 v18, v18
	v_lshlrev_b32_e32 v19, 3, v7
	v_cvt_f32_u32_e32 v19, v19
	s_waitcnt vmcnt(4)
	v_lshlrev_b32_e32 v16, 2, v3
	v_add_u32_e32 v17, 64, v16
	ds_bpermute_b32 v40, v16, v32
	ds_bpermute_b32 v46, v17, v32
	ds_bpermute_b32 v41, v16, v33
	ds_bpermute_b32 v47, v17, v33
	ds_bpermute_b32 v42, v16, v34
	ds_bpermute_b32 v48, v17, v34
	ds_bpermute_b32 v43, v16, v35
	ds_bpermute_b32 v49, v17, v35
	ds_bpermute_b32 v44, v16, v36
	ds_bpermute_b32 v50, v17, v36
	ds_bpermute_b32 v45, v16, v37
	ds_bpermute_b32 v51, v17, v37
	s_waitcnt lgkmcnt(0)
	v_add_f32_e32 v41, v40, v41
	v_sub_f32_e32 v12, v19, v42
	v_sub_f32_e32 v13, v18, v43
	v_rcp_f32_e32 v42, v40
	v_rcp_f32_e32 v43, v41
	s_nop 0
	v_fma_f32 v20, -v40, v42, 1.0
	v_fma_f32 v42, v20, v42, v42
	v_fma_f32 v20, -v41, v43, 1.0
	v_fma_f32 v43, v20, v43, v43
	v_mul_f32_e32 v8, 0xbf38aa3b, v42
	v_mul_f32_e32 v9, 0xbf38aa3b, v43
	v_mul_f32_e32 v44, v44, v42
	v_mul_f32_e32 v45, v45, v43
	v_mul_f32_e32 v10, 0x3e22f983, v44
	v_mul_f32_e32 v11, 0x3e22f983, v45
	v_add_f32_e32 v47, v46, v47
	v_sub_f32_e32 v2, v19, v48
	v_sub_f32_e32 v3, v18, v49
	v_rcp_f32_e32 v48, v46
	v_rcp_f32_e32 v49, v47
	s_nop 0
	v_fma_f32 v20, -v46, v48, 1.0
	v_fma_f32 v48, v20, v48, v48
	v_fma_f32 v20, -v47, v49, 1.0
	v_fma_f32 v49, v20, v49, v49
	v_mul_f32_e32 v28, 0xbf38aa3b, v48
	v_mul_f32_e32 v29, 0xbf38aa3b, v49
	v_mul_f32_e32 v50, v50, v48
	v_mul_f32_e32 v51, v51, v49
	v_mul_f32_e32 v30, 0x3e22f983, v50
	v_mul_f32_e32 v31, 0x3e22f983, v51
	s_getpc_b64 s[44:45]

.Lno_karg_touch:
	v_mul_f32_e32 v16, v12, v12
	v_add_f32_e32 v17, 0x3f800000, v12
	v_add_f32_e32 v18, 0x40000000, v12
	v_add_f32_e32 v19, 0x40400000, v12
	v_mul_f32_e32 v17, v17, v17
	v_mul_f32_e32 v18, v18, v18
	v_mul_f32_e32 v19, v19, v19
	v_mul_f32_e32 v20, v8, v16
	v_mul_f32_e32 v24, v9, v16
	v_mul_f32_e32 v21, v8, v17
	v_mul_f32_e32 v25, v9, v17
	v_mul_f32_e32 v22, v8, v18
	v_mul_f32_e32 v26, v9, v18
	v_mul_f32_e32 v23, v8, v19
	v_mul_f32_e32 v27, v9, v19
	v_exp_f32_e32 v20, v20
	v_exp_f32_e32 v21, v21
	v_exp_f32_e32 v22, v22
	v_exp_f32_e32 v23, v23
	v_exp_f32_e32 v24, v24
	v_exp_f32_e32 v25, v25
	v_exp_f32_e32 v26, v26
	v_exp_f32_e32 v27, v27
	v_cvt_pk_f16_f32 v32, v20, v21
	v_cvt_pk_f16_f32 v33, v22, v23
	v_cvt_pk_f16_f32 v64, v24, v25
	v_cvt_pk_f16_f32 v65, v26, v27
	v_add_f32_e32 v16, 0x40800000, v12
	v_add_f32_e32 v17, 0x40a00000, v12
	v_add_f32_e32 v18, 0x40c00000, v12
	v_add_f32_e32 v19, 0x40e00000, v12
	v_mul_f32_e32 v16, v16, v16
	v_mul_f32_e32 v17, v17, v17
	v_mul_f32_e32 v18, v18, v18
	v_mul_f32_e32 v19, v19, v19
	v_mul_f32_e32 v20, v8, v16
	v_mul_f32_e32 v24, v9, v16
	v_mul_f32_e32 v21, v8, v17
	v_mul_f32_e32 v25, v9, v17
	v_mul_f32_e32 v22, v8, v18
	v_mul_f32_e32 v26, v9, v18
	v_mul_f32_e32 v23, v8, v19
	v_mul_f32_e32 v27, v9, v19
	v_exp_f32_e32 v20, v20
	v_exp_f32_e32 v21, v21
	v_exp_f32_e32 v22, v22
	v_exp_f32_e32 v23, v23
	v_exp_f32_e32 v24, v24
	v_exp_f32_e32 v25, v25
	v_exp_f32_e32 v26, v26
	v_exp_f32_e32 v27, v27
	v_cvt_pk_f16_f32 v34, v20, v21
	v_cvt_pk_f16_f32 v35, v22, v23
	v_cvt_pk_f16_f32 v66, v24, v25
	v_cvt_pk_f16_f32 v67, v26, v27
	v_add_u32_e32 v6, 0x8000, v6
	global_load_dwordx4 v[144:147], v6, s[12:13] offset:0 nt
	global_load_dwordx4 v[148:151], v6, s[12:13] offset:1024 nt
	global_load_dwordx4 v[152:155], v6, s[12:13] offset:2048 nt
	global_load_dwordx4 v[156:159], v6, s[12:13] offset:3072 nt
	v_add_f32_e32 v16, 0x42000000, v12
	v_add_f32_e32 v17, 0x42040000, v12
	v_add_f32_e32 v18, 0x42080000, v12
	v_add_f32_e32 v19, 0x420c0000, v12
	v_mul_f32_e32 v16, v16, v16
	v_mul_f32_e32 v17, v17, v17
	v_mul_f32_e32 v18, v18, v18
	v_mul_f32_e32 v19, v19, v19
	v_mul_f32_e32 v20, v8, v16
	v_mul_f32_e32 v24, v9, v16
	v_mul_f32_e32 v21, v8, v17
	v_mul_f32_e32 v25, v9, v17
	v_mul_f32_e32 v22, v8, v18
	v_mul_f32_e32 v26, v9, v18
	v_mul_f32_e32 v23, v8, v19
	v_mul_f32_e32 v27, v9, v19
	v_exp_f32_e32 v20, v20
	v_exp_f32_e32 v21, v21
	v_exp_f32_e32 v22, v22
	v_exp_f32_e32 v23, v23
	v_exp_f32_e32 v24, v24
	v_exp_f32_e32 v25, v25
	v_exp_f32_e32 v26, v26
	v_exp_f32_e32 v27, v27
	v_cvt_pk_f16_f32 v36, v20, v21
	v_cvt_pk_f16_f32 v37, v22, v23
	v_cvt_pk_f16_f32 v68, v24, v25
	v_cvt_pk_f16_f32 v69, v26, v27
	v_add_f32_e32 v16, 0x42100000, v12
	v_add_f32_e32 v17, 0x42140000, v12
	v_add_f32_e32 v18, 0x42180000, v12
	v_add_f32_e32 v19, 0x421c0000, v12
	v_mul_f32_e32 v16, v16, v16
	v_mul_f32_e32 v17, v17, v17
	v_mul_f32_e32 v18, v18, v18
	v_mul_f32_e32 v19, v19, v19
	v_mul_f32_e32 v20, v8, v16
	v_mul_f32_e32 v24, v9, v16
	v_mul_f32_e32 v21, v8, v17
	v_mul_f32_e32 v25, v9, v17
	v_mul_f32_e32 v22, v8, v18
	v_mul_f32_e32 v26, v9, v18
	v_mul_f32_e32 v23, v8, v19
	v_mul_f32_e32 v27, v9, v19
	v_exp_f32_e32 v20, v20
	v_exp_f32_e32 v21, v21
	v_exp_f32_e32 v22, v22
	v_exp_f32_e32 v23, v23
	v_exp_f32_e32 v24, v24
	v_exp_f32_e32 v25, v25
	v_exp_f32_e32 v26, v26
	v_exp_f32_e32 v27, v27
	v_cvt_pk_f16_f32 v38, v20, v21
	v_cvt_pk_f16_f32 v39, v22, v23
	v_cvt_pk_f16_f32 v70, v24, v25
	v_cvt_pk_f16_f32 v71, v26, v27
	v_add_f32_e32 v16, 0x42800000, v12
	v_add_f32_e32 v17, 0x42820000, v12
	v_add_f32_e32 v18, 0x42840000, v12
	v_add_f32_e32 v19, 0x42860000, v12
	v_mul_f32_e32 v16, v16, v16
	v_mul_f32_e32 v17, v17, v17
	v_mul_f32_e32 v18, v18, v18
	v_mul_f32_e32 v19, v19, v19
	v_mul_f32_e32 v20, v8, v16
	v_mul_f32_e32 v24, v9, v16
	v_mul_f32_e32 v21, v8, v17
	v_mul_f32_e32 v25, v9, v17
	v_mul_f32_e32 v22, v8, v18
	v_mul_f32_e32 v26, v9, v18
	v_mul_f32_e32 v23, v8, v19
	v_mul_f32_e32 v27, v9, v19
	v_exp_f32_e32 v20, v20
	v_exp_f32_e32 v21, v21
	v_exp_f32_e32 v22, v22
	v_exp_f32_e32 v23, v23
	v_exp_f32_e32 v24, v24
	v_exp_f32_e32 v25, v25
	v_exp_f32_e32 v26, v26
	v_exp_f32_e32 v27, v27
	v_cvt_pk_f16_f32 v40, v20, v21
	v_cvt_pk_f16_f32 v41, v22, v23
	v_cvt_pk_f16_f32 v72, v24, v25
	v_cvt_pk_f16_f32 v73, v26, v27
	v_add_f32_e32 v16, 0x42880000, v12
	v_add_f32_e32 v17, 0x428a0000, v12
	v_add_f32_e32 v18, 0x428c0000, v12
	v_add_f32_e32 v19, 0x428e0000, v12
	v_mul_f32_e32 v16, v16, v16
	v_mul_f32_e32 v17, v17, v17
	v_mul_f32_e32 v18, v18, v18
	v_mul_f32_e32 v19, v19, v19
	v_mul_f32_e32 v20, v8, v16
	v_mul_f32_e32 v24, v9, v16
	v_mul_f32_e32 v21, v8, v17
	v_mul_f32_e32 v25, v9, v17
	v_mul_f32_e32 v22, v8, v18
	v_mul_f32_e32 v26, v9, v18
	v_mul_f32_e32 v23, v8, v19
	v_mul_f32_e32 v27, v9, v19
	v_exp_f32_e32 v20, v20
	v_exp_f32_e32 v21, v21
	v_exp_f32_e32 v22, v22
	v_exp_f32_e32 v23, v23
	v_exp_f32_e32 v24, v24
	v_exp_f32_e32 v25, v25
	v_exp_f32_e32 v26, v26
	v_exp_f32_e32 v27, v27
	v_cvt_pk_f16_f32 v42, v20, v21
	v_cvt_pk_f16_f32 v43, v22, v23
	v_cvt_pk_f16_f32 v74, v24, v25
	v_cvt_pk_f16_f32 v75, v26, v27
	v_add_u32_e32 v6, 0x8000, v6
	global_load_dwordx4 v[160:163], v6, s[12:13] offset:0 nt
	global_load_dwordx4 v[164:167], v6, s[12:13] offset:1024 nt
	global_load_dwordx4 v[168:171], v6, s[12:13] offset:2048 nt
	global_load_dwordx4 v[172:175], v6, s[12:13] offset:3072 nt
	v_add_f32_e32 v16, 0x42c00000, v12
	v_add_f32_e32 v17, 0x42c20000, v12
	v_add_f32_e32 v18, 0x42c40000, v12
	v_add_f32_e32 v19, 0x42c60000, v12
	v_mul_f32_e32 v16, v16, v16
	v_mul_f32_e32 v17, v17, v17
	v_mul_f32_e32 v18, v18, v18
	v_mul_f32_e32 v19, v19, v19
	v_mul_f32_e32 v20, v8, v16
	v_mul_f32_e32 v24, v9, v16
	v_mul_f32_e32 v21, v8, v17
	v_mul_f32_e32 v25, v9, v17
	v_mul_f32_e32 v22, v8, v18
	v_mul_f32_e32 v26, v9, v18
	v_mul_f32_e32 v23, v8, v19
	v_mul_f32_e32 v27, v9, v19
	v_exp_f32_e32 v20, v20
	v_exp_f32_e32 v21, v21
	v_exp_f32_e32 v22, v22
	v_exp_f32_e32 v23, v23
	v_exp_f32_e32 v24, v24
	v_exp_f32_e32 v25, v25
	v_exp_f32_e32 v26, v26
	v_exp_f32_e32 v27, v27
	v_cvt_pk_f16_f32 v44, v20, v21
	v_cvt_pk_f16_f32 v45, v22, v23
	v_cvt_pk_f16_f32 v76, v24, v25
	v_cvt_pk_f16_f32 v77, v26, v27
	v_add_f32_e32 v16, 0x42c80000, v12
	v_add_f32_e32 v17, 0x42ca0000, v12
	v_add_f32_e32 v18, 0x42cc0000, v12
	v_add_f32_e32 v19, 0x42ce0000, v12
	v_mul_f32_e32 v16, v16, v16
	v_mul_f32_e32 v17, v17, v17
	v_mul_f32_e32 v18, v18, v18
	v_mul_f32_e32 v19, v19, v19
	v_mul_f32_e32 v20, v8, v16
	v_mul_f32_e32 v24, v9, v16
	v_mul_f32_e32 v21, v8, v17
	v_mul_f32_e32 v25, v9, v17
	v_mul_f32_e32 v22, v8, v18
	v_mul_f32_e32 v26, v9, v18
	v_mul_f32_e32 v23, v8, v19
	v_mul_f32_e32 v27, v9, v19
	v_exp_f32_e32 v20, v20
	v_exp_f32_e32 v21, v21
	v_exp_f32_e32 v22, v22
	v_exp_f32_e32 v23, v23
	v_exp_f32_e32 v24, v24
	v_exp_f32_e32 v25, v25
	v_exp_f32_e32 v26, v26
	v_exp_f32_e32 v27, v27
	v_cvt_pk_f16_f32 v46, v20, v21
	v_cvt_pk_f16_f32 v47, v22, v23
	v_cvt_pk_f16_f32 v78, v24, v25
	v_cvt_pk_f16_f32 v79, v26, v27
	v_mul_f32_e32 v16, v2, v2
	v_add_f32_e32 v17, 0x3f800000, v2
	v_add_f32_e32 v18, 0x40000000, v2
	v_add_f32_e32 v19, 0x40400000, v2
	v_mul_f32_e32 v17, v17, v17
	v_mul_f32_e32 v18, v18, v18
	v_mul_f32_e32 v19, v19, v19
	v_mul_f32_e32 v20, v28, v16
	v_mul_f32_e32 v24, v29, v16
	v_mul_f32_e32 v21, v28, v17
	v_mul_f32_e32 v25, v29, v17
	v_mul_f32_e32 v22, v28, v18
	v_mul_f32_e32 v26, v29, v18
	v_mul_f32_e32 v23, v28, v19
	v_mul_f32_e32 v27, v29, v19
	v_exp_f32_e32 v20, v20
	v_exp_f32_e32 v21, v21
	v_exp_f32_e32 v22, v22
	v_exp_f32_e32 v23, v23
	v_exp_f32_e32 v24, v24
	v_exp_f32_e32 v25, v25
	v_exp_f32_e32 v26, v26
	v_exp_f32_e32 v27, v27
	v_cvt_pk_f16_f32 v48, v20, v21
	v_cvt_pk_f16_f32 v49, v22, v23
	v_cvt_pk_f16_f32 v80, v24, v25
	v_cvt_pk_f16_f32 v81, v26, v27
	v_add_f32_e32 v16, 0x40800000, v2
	v_add_f32_e32 v17, 0x40a00000, v2
	v_add_f32_e32 v18, 0x40c00000, v2
	v_add_f32_e32 v19, 0x40e00000, v2
	v_mul_f32_e32 v16, v16, v16
	v_mul_f32_e32 v17, v17, v17
	v_mul_f32_e32 v18, v18, v18
	v_mul_f32_e32 v19, v19, v19
	v_mul_f32_e32 v20, v28, v16
	v_mul_f32_e32 v24, v29, v16
	v_mul_f32_e32 v21, v28, v17
	v_mul_f32_e32 v25, v29, v17
	v_mul_f32_e32 v22, v28, v18
	v_mul_f32_e32 v26, v29, v18
	v_mul_f32_e32 v23, v28, v19
	v_mul_f32_e32 v27, v29, v19
	v_exp_f32_e32 v20, v20
	v_exp_f32_e32 v21, v21
	v_exp_f32_e32 v22, v22
	v_exp_f32_e32 v23, v23
	v_exp_f32_e32 v24, v24
	v_exp_f32_e32 v25, v25
	v_exp_f32_e32 v26, v26
	v_exp_f32_e32 v27, v27
	v_cvt_pk_f16_f32 v50, v20, v21
	v_cvt_pk_f16_f32 v51, v22, v23
	v_cvt_pk_f16_f32 v82, v24, v25
	v_cvt_pk_f16_f32 v83, v26, v27
	v_add_u32_e32 v6, 0x8000, v6
	global_load_dwordx4 v[176:179], v6, s[12:13] offset:0 nt
	global_load_dwordx4 v[180:183], v6, s[12:13] offset:1024 nt
	global_load_dwordx4 v[184:187], v6, s[12:13] offset:2048 nt
	global_load_dwordx4 v[188:191], v6, s[12:13] offset:3072 nt
	v_add_f32_e32 v16, 0x42000000, v2
	v_add_f32_e32 v17, 0x42040000, v2
	v_add_f32_e32 v18, 0x42080000, v2
	v_add_f32_e32 v19, 0x420c0000, v2
	v_mul_f32_e32 v16, v16, v16
	v_mul_f32_e32 v17, v17, v17
	v_mul_f32_e32 v18, v18, v18
	v_mul_f32_e32 v19, v19, v19
	v_mul_f32_e32 v20, v28, v16
	v_mul_f32_e32 v24, v29, v16
	v_mul_f32_e32 v21, v28, v17
	v_mul_f32_e32 v25, v29, v17
	v_mul_f32_e32 v22, v28, v18
	v_mul_f32_e32 v26, v29, v18
	v_mul_f32_e32 v23, v28, v19
	v_mul_f32_e32 v27, v29, v19
	v_exp_f32_e32 v20, v20
	v_exp_f32_e32 v21, v21
	v_exp_f32_e32 v22, v22
	v_exp_f32_e32 v23, v23
	v_exp_f32_e32 v24, v24
	v_exp_f32_e32 v25, v25
	v_exp_f32_e32 v26, v26
	v_exp_f32_e32 v27, v27
	v_cvt_pk_f16_f32 v52, v20, v21
	v_cvt_pk_f16_f32 v53, v22, v23
	v_cvt_pk_f16_f32 v84, v24, v25
	v_cvt_pk_f16_f32 v85, v26, v27
	v_add_f32_e32 v16, 0x42100000, v2
	v_add_f32_e32 v17, 0x42140000, v2
	v_add_f32_e32 v18, 0x42180000, v2
	v_add_f32_e32 v19, 0x421c0000, v2
	v_mul_f32_e32 v16, v16, v16
	v_mul_f32_e32 v17, v17, v17
	v_mul_f32_e32 v18, v18, v18
	v_mul_f32_e32 v19, v19, v19
	v_mul_f32_e32 v20, v28, v16
	v_mul_f32_e32 v24, v29, v16
	v_mul_f32_e32 v21, v28, v17
	v_mul_f32_e32 v25, v29, v17
	v_mul_f32_e32 v22, v28, v18
	v_mul_f32_e32 v26, v29, v18
	v_mul_f32_e32 v23, v28, v19
	v_mul_f32_e32 v27, v29, v19
	v_exp_f32_e32 v20, v20
	v_exp_f32_e32 v21, v21
	v_exp_f32_e32 v22, v22
	v_exp_f32_e32 v23, v23
	v_exp_f32_e32 v24, v24
	v_exp_f32_e32 v25, v25
	v_exp_f32_e32 v26, v26
	v_exp_f32_e32 v27, v27
	v_cvt_pk_f16_f32 v54, v20, v21
	v_cvt_pk_f16_f32 v55, v22, v23
	v_cvt_pk_f16_f32 v86, v24, v25
	v_cvt_pk_f16_f32 v87, v26, v27
	v_add_f32_e32 v16, 0x42800000, v2
	v_add_f32_e32 v17, 0x42820000, v2
	v_add_f32_e32 v18, 0x42840000, v2
	v_add_f32_e32 v19, 0x42860000, v2
	v_mul_f32_e32 v16, v16, v16
	v_mul_f32_e32 v17, v17, v17
	v_mul_f32_e32 v18, v18, v18
	v_mul_f32_e32 v19, v19, v19
	v_mul_f32_e32 v20, v28, v16
	v_mul_f32_e32 v24, v29, v16
	v_mul_f32_e32 v21, v28, v17
	v_mul_f32_e32 v25, v29, v17
	v_mul_f32_e32 v22, v28, v18
	v_mul_f32_e32 v26, v29, v18
	v_mul_f32_e32 v23, v28, v19
	v_mul_f32_e32 v27, v29, v19
	v_exp_f32_e32 v20, v20
	v_exp_f32_e32 v21, v21
	v_exp_f32_e32 v22, v22
	v_exp_f32_e32 v23, v23
	v_exp_f32_e32 v24, v24
	v_exp_f32_e32 v25, v25
	v_exp_f32_e32 v26, v26
	v_exp_f32_e32 v27, v27
	v_cvt_pk_f16_f32 v56, v20, v21
	v_cvt_pk_f16_f32 v57, v22, v23
	v_cvt_pk_f16_f32 v88, v24, v25
	v_cvt_pk_f16_f32 v89, v26, v27
	v_add_f32_e32 v16, 0x42880000, v2
	v_add_f32_e32 v17, 0x428a0000, v2
	v_add_f32_e32 v18, 0x428c0000, v2
	v_add_f32_e32 v19, 0x428e0000, v2
	v_mul_f32_e32 v16, v16, v16
	v_mul_f32_e32 v17, v17, v17
	v_mul_f32_e32 v18, v18, v18
	v_mul_f32_e32 v19, v19, v19
	v_mul_f32_e32 v20, v28, v16
	v_mul_f32_e32 v24, v29, v16
	v_mul_f32_e32 v21, v28, v17
	v_mul_f32_e32 v25, v29, v17
	v_mul_f32_e32 v22, v28, v18
	v_mul_f32_e32 v26, v29, v18
	v_mul_f32_e32 v23, v28, v19
	v_mul_f32_e32 v27, v29, v19
	v_exp_f32_e32 v20, v20
	v_exp_f32_e32 v21, v21
	v_exp_f32_e32 v22, v22
	v_exp_f32_e32 v23, v23
	v_exp_f32_e32 v24, v24
	v_exp_f32_e32 v25, v25
	v_exp_f32_e32 v26, v26
	v_exp_f32_e32 v27, v27
	v_cvt_pk_f16_f32 v58, v20, v21
	v_cvt_pk_f16_f32 v59, v22, v23
	v_cvt_pk_f16_f32 v90, v24, v25
	v_cvt_pk_f16_f32 v91, v26, v27
	v_add_u32_e32 v6, 0x8000, v6
	global_load_dwordx4 v[192:195], v6, s[12:13] offset:0 nt
	global_load_dwordx4 v[196:199], v6, s[12:13] offset:1024 nt
	global_load_dwordx4 v[200:203], v6, s[12:13] offset:2048 nt
	global_load_dwordx4 v[204:207], v6, s[12:13] offset:3072 nt
	v_add_f32_e32 v16, 0x42c00000, v2
	v_add_f32_e32 v17, 0x42c20000, v2
	v_add_f32_e32 v18, 0x42c40000, v2
	v_add_f32_e32 v19, 0x42c60000, v2
	v_mul_f32_e32 v16, v16, v16
	v_mul_f32_e32 v17, v17, v17
	v_mul_f32_e32 v18, v18, v18
	v_mul_f32_e32 v19, v19, v19
	v_mul_f32_e32 v20, v28, v16
	v_mul_f32_e32 v24, v29, v16
	v_mul_f32_e32 v21, v28, v17
	v_mul_f32_e32 v25, v29, v17
	v_mul_f32_e32 v22, v28, v18
	v_mul_f32_e32 v26, v29, v18
	v_mul_f32_e32 v23, v28, v19
	v_mul_f32_e32 v27, v29, v19
	v_exp_f32_e32 v20, v20
	v_exp_f32_e32 v21, v21
	v_exp_f32_e32 v22, v22
	v_exp_f32_e32 v23, v23
	v_exp_f32_e32 v24, v24
	v_exp_f32_e32 v25, v25
	v_exp_f32_e32 v26, v26
	v_exp_f32_e32 v27, v27
	v_cvt_pk_f16_f32 v60, v20, v21
	v_cvt_pk_f16_f32 v61, v22, v23
	v_cvt_pk_f16_f32 v92, v24, v25
	v_cvt_pk_f16_f32 v93, v26, v27
	v_add_f32_e32 v16, 0x42c80000, v2
	v_add_f32_e32 v17, 0x42ca0000, v2
	v_add_f32_e32 v18, 0x42cc0000, v2
	v_add_f32_e32 v19, 0x42ce0000, v2
	v_mul_f32_e32 v16, v16, v16
	v_mul_f32_e32 v17, v17, v17
	v_mul_f32_e32 v18, v18, v18
	v_mul_f32_e32 v19, v19, v19
	v_mul_f32_e32 v20, v28, v16
	v_mul_f32_e32 v24, v29, v16
	v_mul_f32_e32 v21, v28, v17
	v_mul_f32_e32 v25, v29, v17
	v_mul_f32_e32 v22, v28, v18
	v_mul_f32_e32 v26, v29, v18
	v_mul_f32_e32 v23, v28, v19
	v_mul_f32_e32 v27, v29, v19
	v_exp_f32_e32 v20, v20
	v_exp_f32_e32 v21, v21
	v_exp_f32_e32 v22, v22
	v_exp_f32_e32 v23, v23
	v_exp_f32_e32 v24, v24
	v_exp_f32_e32 v25, v25
	v_exp_f32_e32 v26, v26
	v_exp_f32_e32 v27, v27
	v_cvt_pk_f16_f32 v62, v20, v21
	v_cvt_pk_f16_f32 v63, v22, v23
	v_cvt_pk_f16_f32 v94, v24, v25
	v_cvt_pk_f16_f32 v95, v26, v27
	v_mul_f32_e32 v16, v13, v13
	v_add_f32_e32 v17, 0x3f800000, v13
	v_add_f32_e32 v18, 0x40000000, v13
	v_add_f32_e32 v19, 0x40400000, v13
	v_mul_f32_e32 v17, v17, v17
	v_mul_f32_e32 v18, v18, v18
	v_mul_f32_e32 v19, v19, v19
	v_mul_f32_e32 v20, v8, v16
	v_mul_f32_e32 v24, v9, v16
	v_mul_f32_e32 v21, v8, v17
	v_mul_f32_e32 v25, v9, v17
	v_mul_f32_e32 v22, v8, v18
	v_mul_f32_e32 v26, v9, v18
	v_mul_f32_e32 v23, v8, v19
	v_mul_f32_e32 v27, v9, v19
	v_exp_f32_e32 v20, v20
	v_exp_f32_e32 v21, v21
	v_exp_f32_e32 v22, v22
	v_exp_f32_e32 v23, v23
	v_exp_f32_e32 v24, v24
	v_exp_f32_e32 v25, v25
	v_exp_f32_e32 v26, v26
	v_exp_f32_e32 v27, v27
	v_mul_f32_e32 v96, v10, v20
	v_mul_f32_e32 v97, v10, v21
	v_mul_f32_e32 v98, v10, v22
	v_mul_f32_e32 v99, v10, v23
	v_mul_f32_e32 v112, v11, v24
	v_mul_f32_e32 v113, v11, v25
	v_mul_f32_e32 v114, v11, v26
	v_mul_f32_e32 v115, v11, v27
	v_add_u32_e32 v6, 0x8000, v6
	global_load_dwordx4 v[208:211], v6, s[12:13] offset:0 nt
	global_load_dwordx4 v[212:215], v6, s[12:13] offset:1024 nt
	global_load_dwordx4 v[216:219], v6, s[12:13] offset:2048 nt
	global_load_dwordx4 v[220:223], v6, s[12:13] offset:3072 nt
	v_add_f32_e32 v16, 0x41800000, v13
	v_add_f32_e32 v17, 0x41880000, v13
	v_add_f32_e32 v18, 0x41900000, v13
	v_add_f32_e32 v19, 0x41980000, v13
	v_mul_f32_e32 v16, v16, v16
	v_mul_f32_e32 v17, v17, v17
	v_mul_f32_e32 v18, v18, v18
	v_mul_f32_e32 v19, v19, v19
	v_mul_f32_e32 v20, v8, v16
	v_mul_f32_e32 v24, v9, v16
	v_mul_f32_e32 v21, v8, v17
	v_mul_f32_e32 v25, v9, v17
	v_mul_f32_e32 v22, v8, v18
	v_mul_f32_e32 v26, v9, v18
	v_mul_f32_e32 v23, v8, v19
	v_mul_f32_e32 v27, v9, v19
	v_exp_f32_e32 v20, v20
	v_exp_f32_e32 v21, v21
	v_exp_f32_e32 v22, v22
	v_exp_f32_e32 v23, v23
	v_exp_f32_e32 v24, v24
	v_exp_f32_e32 v25, v25
	v_exp_f32_e32 v26, v26
	v_exp_f32_e32 v27, v27
	v_mul_f32_e32 v100, v10, v20
	v_mul_f32_e32 v101, v10, v21
	v_mul_f32_e32 v102, v10, v22
	v_mul_f32_e32 v103, v10, v23
	v_mul_f32_e32 v116, v11, v24
	v_mul_f32_e32 v117, v11, v25
	v_mul_f32_e32 v118, v11, v26
	v_mul_f32_e32 v119, v11, v27
	v_add_u32_e32 v6, 0x8000, v6
	global_load_dwordx4 v[224:227], v6, s[12:13] offset:0 nt
	global_load_dwordx4 v[228:231], v6, s[12:13] offset:1024 nt
	global_load_dwordx4 v[232:235], v6, s[12:13] offset:2048 nt
	global_load_dwordx4 v[236:239], v6, s[12:13] offset:3072 nt
	v_mul_f32_e32 v16, v3, v3
	v_add_f32_e32 v17, 0x3f800000, v3
	v_add_f32_e32 v18, 0x40000000, v3
	v_add_f32_e32 v19, 0x40400000, v3
	v_mul_f32_e32 v17, v17, v17
	v_mul_f32_e32 v18, v18, v18
	v_mul_f32_e32 v19, v19, v19
	v_mul_f32_e32 v20, v28, v16
	v_mul_f32_e32 v24, v29, v16
	v_mul_f32_e32 v21, v28, v17
	v_mul_f32_e32 v25, v29, v17
	v_mul_f32_e32 v22, v28, v18
	v_mul_f32_e32 v26, v29, v18
	v_mul_f32_e32 v23, v28, v19
	v_mul_f32_e32 v27, v29, v19
	v_exp_f32_e32 v20, v20
	v_exp_f32_e32 v21, v21
	v_exp_f32_e32 v22, v22
	v_exp_f32_e32 v23, v23
	v_exp_f32_e32 v24, v24
	v_exp_f32_e32 v25, v25
	v_exp_f32_e32 v26, v26
	v_exp_f32_e32 v27, v27
	v_mul_f32_e32 v104, v30, v20
	v_mul_f32_e32 v105, v30, v21
	v_mul_f32_e32 v106, v30, v22
	v_mul_f32_e32 v107, v30, v23
	v_mul_f32_e32 v120, v31, v24
	v_mul_f32_e32 v121, v31, v25
	v_mul_f32_e32 v122, v31, v26
	v_mul_f32_e32 v123, v31, v27
	v_add_f32_e32 v16, 0x41800000, v3
	v_add_f32_e32 v17, 0x41880000, v3
	v_add_f32_e32 v18, 0x41900000, v3
	v_add_f32_e32 v19, 0x41980000, v3
	v_mul_f32_e32 v16, v16, v16
	v_mul_f32_e32 v17, v17, v17
	v_mul_f32_e32 v18, v18, v18
	v_mul_f32_e32 v19, v19, v19
	v_mul_f32_e32 v20, v28, v16
	v_mul_f32_e32 v24, v29, v16
	v_mul_f32_e32 v21, v28, v17
	v_mul_f32_e32 v25, v29, v17
	v_mul_f32_e32 v22, v28, v18
	v_mul_f32_e32 v26, v29, v18
	v_mul_f32_e32 v23, v28, v19
	v_mul_f32_e32 v27, v29, v19
	v_exp_f32_e32 v20, v20
	v_exp_f32_e32 v21, v21
	v_exp_f32_e32 v22, v22
	v_exp_f32_e32 v23, v23
	v_exp_f32_e32 v24, v24
	v_exp_f32_e32 v25, v25
	v_exp_f32_e32 v26, v26
	v_exp_f32_e32 v27, v27
	v_mul_f32_e32 v108, v30, v20
	v_mul_f32_e32 v109, v30, v21
	v_mul_f32_e32 v110, v30, v22
	v_mul_f32_e32 v111, v30, v23
	v_mul_f32_e32 v124, v31, v24
	v_mul_f32_e32 v125, v31, v25
	v_mul_f32_e32 v126, v31, v26
	v_mul_f32_e32 v127, v31, v27
	v_add_u32_e32 v6, 0x8000, v6
	global_load_dwordx4 v[240:243], v6, s[12:13] offset:0 nt
	global_load_dwordx4 v[244:247], v6, s[12:13] offset:1024 nt
	global_load_dwordx4 v[248:251], v6, s[12:13] offset:2048 nt
	global_load_dwordx4 v[252:255], v6, s[12:13] offset:3072 nt
	s_waitcnt vmcnt(28)
	v_add_f32_e32 v128, v128, v129
	v_add_f32_e32 v130, v130, v131
	v_add_f32_e32 v132, v132, v133
	v_add_f32_e32 v134, v134, v135
	v_add_f32_e32 v136, v136, v137
	v_add_f32_e32 v138, v138, v139
	v_add_f32_e32 v140, v140, v141
	v_add_f32_e32 v142, v142, v143
	v_add_f32_e32 v128, v128, v130
	v_add_f32_e32 v132, v132, v134
	v_add_f32_e32 v136, v136, v138
	v_add_f32_e32 v140, v140, v142
	v_cndmask_b32_e64 v130, v128, v132, s[30:31]
	v_cndmask_b32_e64 v134, v136, v140, s[30:31]
	v_cndmask_b32_e64 v129, v132, v128, s[30:31]
	v_cndmask_b32_e64 v133, v140, v136, s[30:31]
	v_add_f32_dpp v129, v130, v129 quad_perm:[1,0,3,2] row_mask:0xf bank_mask:0xf bound_ctrl:1
	v_add_f32_dpp v133, v134, v133 quad_perm:[1,0,3,2] row_mask:0xf bank_mask:0xf bound_ctrl:1
	v_cndmask_b32_e64 v135, v129, v133, s[32:33]
	v_cndmask_b32_e64 v131, v133, v129, s[32:33]
	s_nop 1
	v_add_f32_dpp v131, v135, v131 quad_perm:[2,3,0,1] row_mask:0xf bank_mask:0xf bound_ctrl:1
	v_cvt_f16_f32_e32 v131, v131
	ds_write_b16 v14, v131 offset:0
	s_waitcnt vmcnt(24)
	v_add_f32_e32 v144, v144, v145
	v_add_f32_e32 v146, v146, v147
	v_add_f32_e32 v148, v148, v149
	v_add_f32_e32 v150, v150, v151
	v_add_f32_e32 v152, v152, v153
	v_add_f32_e32 v154, v154, v155
	v_add_f32_e32 v156, v156, v157
	v_add_f32_e32 v158, v158, v159
	v_add_f32_e32 v144, v144, v146
	v_add_f32_e32 v148, v148, v150
	v_add_f32_e32 v152, v152, v154
	v_add_f32_e32 v156, v156, v158
	v_cndmask_b32_e64 v146, v144, v148, s[30:31]
	v_cndmask_b32_e64 v150, v152, v156, s[30:31]
	v_cndmask_b32_e64 v145, v148, v144, s[30:31]
	v_cndmask_b32_e64 v149, v156, v152, s[30:31]
	v_add_f32_dpp v145, v146, v145 quad_perm:[1,0,3,2] row_mask:0xf bank_mask:0xf bound_ctrl:1
	v_add_f32_dpp v149, v150, v149 quad_perm:[1,0,3,2] row_mask:0xf bank_mask:0xf bound_ctrl:1
	v_cndmask_b32_e64 v151, v145, v149, s[32:33]
	v_cndmask_b32_e64 v147, v149, v145, s[32:33]
	s_nop 1
	v_add_f32_dpp v147, v151, v147 quad_perm:[2,3,0,1] row_mask:0xf bank_mask:0xf bound_ctrl:1
	v_cvt_f16_f32_e32 v147, v147
	ds_write_b16 v14, v147 offset:1088
	s_waitcnt vmcnt(20)
	v_add_f32_e32 v160, v160, v161
	v_add_f32_e32 v162, v162, v163
	v_add_f32_e32 v164, v164, v165
	v_add_f32_e32 v166, v166, v167
	v_add_f32_e32 v168, v168, v169
	v_add_f32_e32 v170, v170, v171
	v_add_f32_e32 v172, v172, v173
	v_add_f32_e32 v174, v174, v175
	v_add_f32_e32 v160, v160, v162
	v_add_f32_e32 v164, v164, v166
	v_add_f32_e32 v168, v168, v170
	v_add_f32_e32 v172, v172, v174
	v_cndmask_b32_e64 v162, v160, v164, s[30:31]
	v_cndmask_b32_e64 v166, v168, v172, s[30:31]
	v_cndmask_b32_e64 v161, v164, v160, s[30:31]
	v_cndmask_b32_e64 v165, v172, v168, s[30:31]
	v_add_f32_dpp v161, v162, v161 quad_perm:[1,0,3,2] row_mask:0xf bank_mask:0xf bound_ctrl:1
	v_add_f32_dpp v165, v166, v165 quad_perm:[1,0,3,2] row_mask:0xf bank_mask:0xf bound_ctrl:1
	v_cndmask_b32_e64 v167, v161, v165, s[32:33]
	v_cndmask_b32_e64 v163, v165, v161, s[32:33]
	s_nop 1
	v_add_f32_dpp v163, v167, v163 quad_perm:[2,3,0,1] row_mask:0xf bank_mask:0xf bound_ctrl:1
	v_cvt_f16_f32_e32 v163, v163
	ds_write_b16 v14, v163 offset:2176
	s_waitcnt vmcnt(16)
	v_add_f32_e32 v176, v176, v177
	v_add_f32_e32 v178, v178, v179
	v_add_f32_e32 v180, v180, v181
	v_add_f32_e32 v182, v182, v183
	v_add_f32_e32 v184, v184, v185
	v_add_f32_e32 v186, v186, v187
	v_add_f32_e32 v188, v188, v189
	v_add_f32_e32 v190, v190, v191
	v_add_f32_e32 v176, v176, v178
	v_add_f32_e32 v180, v180, v182
	v_add_f32_e32 v184, v184, v186
	v_add_f32_e32 v188, v188, v190
	v_cndmask_b32_e64 v178, v176, v180, s[30:31]
	v_cndmask_b32_e64 v182, v184, v188, s[30:31]
	v_cndmask_b32_e64 v177, v180, v176, s[30:31]
	v_cndmask_b32_e64 v181, v188, v184, s[30:31]
	v_add_f32_dpp v177, v178, v177 quad_perm:[1,0,3,2] row_mask:0xf bank_mask:0xf bound_ctrl:1
	v_add_f32_dpp v181, v182, v181 quad_perm:[1,0,3,2] row_mask:0xf bank_mask:0xf bound_ctrl:1
	v_cndmask_b32_e64 v183, v177, v181, s[32:33]
	v_cndmask_b32_e64 v179, v181, v177, s[32:33]
	s_nop 1
	v_add_f32_dpp v179, v183, v179 quad_perm:[2,3,0,1] row_mask:0xf bank_mask:0xf bound_ctrl:1
	v_cvt_f16_f32_e32 v179, v179
	ds_write_b16 v14, v179 offset:3264
	s_mov_b32 s29, 0
	v_mov_b32_e32 v160, 0
	v_mov_b32_e32 v161, 0
	v_mov_b32_e32 v162, 0
	v_mov_b32_e32 v163, 0
	s_lshl_b32 s6, s6, 6
	s_add_i32 s6, s6, s7
	s_lshl_b32 s6, s6, 10
	v_add_u32_e32 v5, s6, v5
	s_branch .Lpass
